# speedup vs baseline: 1.0202x; 1.0202x over previous
_Z10rnn_kernelPKDF16_S0_PDF16_S1_:
	s_load_dwordx8 s[4:11], s[0:1], 0x0
	v_readfirstlane_b32 s0, v0
	s_lshr_b32 s12, s0, 6
	s_lshl_b32 s0, s12, 4
	s_mov_b32 s1, 0
	s_lshl_b64 s[14:15], s[0:1], 13
	v_and_b32_e32 v1, 63, v0
	s_waitcnt lgkmcnt(0)
	s_add_u32 s6, s6, s14
	s_addc_u32 s7, s7, s15
	v_lshlrev_b32_e32 v142, 4, v1
	v_mov_b32_e32 v143, 0
	v_lshl_add_u64 v[2:3], s[6:7], 0, v[142:143]
	s_movk_i32 s3, 0x1000
	v_add_co_u32_e32 v4, vcc, s3, v2
	s_mov_b32 s13, 0x18000
	s_nop 0
	v_addc_co_u32_e32 v5, vcc, 0, v3, vcc
	v_add_co_u32_e32 v110, vcc, s13, v2
	s_mov_b32 s13, 0x19000
	s_nop 0
	v_addc_co_u32_e32 v111, vcc, 0, v3, vcc
	v_add_co_u32_e32 v50, vcc, s13, v2
	s_mov_b32 s13, 0x1a000
	s_nop 0
	v_addc_co_u32_e32 v51, vcc, 0, v3, vcc
	v_add_co_u32_e32 v52, vcc, s13, v2
	s_movk_i32 s3, 0x2000
	s_nop 0
	v_addc_co_u32_e32 v53, vcc, 0, v3, vcc
	v_add_co_u32_e32 v54, vcc, s3, v2
	s_movk_i32 s3, 0x3000
	s_nop 0
	v_addc_co_u32_e32 v55, vcc, 0, v3, vcc
	global_load_dwordx4 v[6:9], v[110:111], off
	global_load_dwordx4 v[10:13], v[110:111], off offset:1024
	global_load_dwordx4 v[14:17], v[110:111], off offset:2048
	global_load_dwordx4 v[18:21], v[110:111], off offset:3072
	global_load_dwordx4 v[22:25], v[50:51], off offset:1024
	global_load_dwordx4 v[26:29], v[50:51], off offset:2048
	global_load_dwordx4 a[0:3], v[4:5], off offset:1024
	global_load_dwordx4 a[4:7], v[4:5], off offset:2048
	global_load_dwordx4 a[8:11], v[54:55], off offset:-4096
	global_load_dwordx4 a[12:15], v[54:55], off
	global_load_dwordx4 a[16:19], v[54:55], off offset:1024
	global_load_dwordx4 a[20:23], v[54:55], off offset:2048
	global_load_dwordx4 v[30:33], v[50:51], off offset:3072
	global_load_dwordx4 v[34:37], v[52:53], off offset:-4096
	global_load_dwordx4 v[38:41], v[52:53], off
	global_load_dwordx4 v[42:45], v[52:53], off offset:1024
	global_load_dwordx4 v[46:49], v[52:53], off offset:2048
	v_add_co_u32_e32 v50, vcc, s3, v2
	s_movk_i32 s3, 0x4000
	s_nop 0
	v_addc_co_u32_e32 v51, vcc, 0, v3, vcc
	v_add_co_u32_e32 v56, vcc, s3, v2
	s_movk_i32 s3, 0x5000
	s_nop 0
	v_addc_co_u32_e32 v57, vcc, 0, v3, vcc
	global_load_dwordx4 a[24:27], v[54:55], off offset:3072
	global_load_dwordx4 a[28:31], v[56:57], off offset:-4096
	global_load_dwordx4 a[32:35], v[4:5], off offset:3072
	global_load_dwordx4 a[36:39], v[50:51], off offset:1024
	global_load_dwordx4 a[40:43], v[50:51], off offset:2048
	global_load_dwordx4 a[44:47], v[50:51], off offset:3072
	global_load_dwordx4 a[48:51], v[56:57], off
	global_load_dwordx4 a[52:55], v[56:57], off offset:1024
	global_load_dwordx4 a[56:59], v[56:57], off offset:2048
	global_load_dwordx4 a[60:63], v[56:57], off offset:3072
	v_add_co_u32_e32 v4, vcc, s3, v2
	s_movk_i32 s3, 0x6000
	s_nop 0
	v_addc_co_u32_e32 v5, vcc, 0, v3, vcc
	v_add_co_u32_e32 v98, vcc, s3, v2
	s_movk_i32 s3, 0x7000
	s_nop 0
	v_addc_co_u32_e32 v99, vcc, 0, v3, vcc
	v_add_co_u32_e32 v100, vcc, s3, v2
	s_mov_b32 s3, 0x8000
	s_nop 0
	v_addc_co_u32_e32 v101, vcc, 0, v3, vcc
	global_load_dwordx4 v[50:53], v[52:53], off offset:3072
	v_add_co_u32_e32 v102, vcc, s3, v2
	s_mov_b32 s14, 0x1c000
	s_nop 0
	v_addc_co_u32_e32 v103, vcc, 0, v3, vcc
	v_add_co_u32_e32 v82, vcc, s14, v2
	global_load_dwordx4 a[64:67], v[4:5], off offset:1024
	global_load_dwordx4 a[68:71], v[4:5], off offset:2048
	global_load_dwordx4 a[72:75], v[98:99], off offset:-4096
	global_load_dwordx4 a[76:79], v[98:99], off
	global_load_dwordx4 a[80:83], v[98:99], off offset:1024
	global_load_dwordx4 a[84:87], v[98:99], off offset:2048
	v_addc_co_u32_e32 v83, vcc, 0, v3, vcc
	global_load_dwordx4 v[54:57], v[82:83], off offset:-4096
	s_mov_b32 s13, 0x1b000
	v_add_co_u32_e32 v66, vcc, s13, v2
	s_mov_b32 s13, 0x1d000
	s_nop 0
	v_addc_co_u32_e32 v67, vcc, 0, v3, vcc
	global_load_dwordx4 v[58:61], v[66:67], off offset:1024
	global_load_dwordx4 v[62:65], v[66:67], off offset:2048
	s_nop 0
	global_load_dwordx4 v[66:69], v[66:67], off offset:3072
	s_nop 0
	global_load_dwordx4 v[70:73], v[82:83], off
	global_load_dwordx4 v[74:77], v[82:83], off offset:1024
	global_load_dwordx4 v[78:81], v[82:83], off offset:2048
	s_nop 0
	global_load_dwordx4 v[82:85], v[82:83], off offset:3072
	v_add_co_u32_e32 v104, vcc, s13, v2
	s_mov_b32 s13, 0x1e000
	s_nop 0
	v_addc_co_u32_e32 v105, vcc, 0, v3, vcc
	v_add_co_u32_e32 v106, vcc, s13, v2
	s_lshl_b32 s13, s12, 15
	s_nop 0
	v_addc_co_u32_e32 v107, vcc, 0, v3, vcc
	global_load_dwordx4 v[86:89], v[106:107], off offset:-4096
	global_load_dwordx4 v[90:93], v[104:105], off offset:1024
	global_load_dwordx4 v[94:97], v[104:105], off offset:2048
	global_load_dwordx4 a[88:91], v[98:99], off offset:3072
	global_load_dwordx4 a[92:95], v[102:103], off offset:-4096
	global_load_dwordx4 a[96:99], v[4:5], off offset:3072
	global_load_dwordx4 a[100:103], v[100:101], off offset:1024
	global_load_dwordx4 a[104:107], v[100:101], off offset:2048
	global_load_dwordx4 a[108:111], v[100:101], off offset:3072
	global_load_dwordx4 a[112:115], v[102:103], off
	global_load_dwordx4 a[116:119], v[102:103], off offset:1024
	global_load_dwordx4 a[120:123], v[102:103], off offset:2048
	global_load_dwordx4 a[124:127], v[102:103], off offset:3072
	s_add_i32 s13, s13, 0
	v_add_u32_e32 v213, s13, v142
	s_mov_b32 s13, 0x9000
	s_waitcnt vmcnt(54)
	ds_write_b128 v213, v[6:9]
	s_waitcnt vmcnt(53)
	ds_write_b128 v213, v[10:13] offset:1024
	s_waitcnt vmcnt(52)
	ds_write_b128 v213, v[14:17] offset:2048
	s_waitcnt vmcnt(51)
	ds_write_b128 v213, v[18:21] offset:3072
	s_waitcnt vmcnt(41)
	ds_write_b128 v213, v[34:37] offset:4096
	ds_write_b128 v213, v[22:25] offset:5120
	ds_write_b128 v213, v[26:29] offset:6144
	ds_write_b128 v213, v[30:33] offset:7168
	s_waitcnt vmcnt(40)
	ds_write_b128 v213, v[38:41] offset:8192
	s_waitcnt vmcnt(39)
	ds_write_b128 v213, v[42:45] offset:9216
	s_waitcnt vmcnt(38)
	ds_write_b128 v213, v[46:49] offset:10240
	v_add_co_u32_e32 v8, vcc, s13, v2
	s_mov_b32 s13, 0xa000
	s_nop 0
	v_addc_co_u32_e32 v9, vcc, 0, v3, vcc
	v_add_co_u32_e32 v10, vcc, s13, v2
	s_mov_b32 s13, 0xb000
	s_nop 0
	v_addc_co_u32_e32 v11, vcc, 0, v3, vcc
	v_add_co_u32_e32 v12, vcc, s13, v2
	s_mov_b32 s13, 0xc000
	s_nop 0
	v_addc_co_u32_e32 v13, vcc, 0, v3, vcc
	v_and_b32_e32 v32, 15, v0
	v_lshl_or_b32 v206, s2, 4, v32
	v_ashrrev_i32_e32 v207, 31, v206
	v_bfe_u32 v1, v0, 5, 1
	v_lshlrev_b64 v[144:145], 10, v[206:207]
	v_or_b32_e32 v33, s0, v1
	v_bitop3_b32 v1, v1, v32, s0 bitop3:0x36
	s_lshl_b32 s0, s12, 8
	s_mov_b32 s2, 0x400000
	v_bitop3_b32 v153, v33, v32, 12 bitop3:0x36
	v_bitop3_b32 v154, v33, v32, 14 bitop3:0x36
	s_waitcnt vmcnt(27)
	ds_write_b128 v213, v[50:53] offset:11264
	global_load_dwordx4 a[128:131], v[8:9], off offset:1024
	global_load_dwordx4 a[132:135], v[8:9], off offset:2048
	global_load_dwordx4 a[136:139], v[10:11], off offset:-4096
	global_load_dwordx4 a[140:143], v[10:11], off
	global_load_dwordx4 v[4:7], v[104:105], off offset:3072
	global_load_dwordx4 a[144:147], v[10:11], off offset:1024
	global_load_dwordx4 a[148:151], v[10:11], off offset:2048
	global_load_dwordx4 a[152:155], v[8:9], off offset:3072
	global_load_dwordx4 a[156:159], v[12:13], off offset:1024
	global_load_dwordx4 a[160:163], v[12:13], off offset:2048
	global_load_dwordx4 a[164:167], v[12:13], off offset:3072
	v_add_co_u32_e32 v12, vcc, s13, v2
	v_bfe_u32 v218, v0, 4, 2
	s_nop 0
	v_addc_co_u32_e32 v13, vcc, 0, v3, vcc
	global_load_dwordx4 a[168:171], v[10:11], off offset:3072
	global_load_dwordx4 a[172:175], v[12:13], off offset:-4096
	s_waitcnt vmcnt(33)
	ds_write_b128 v213, v[54:57] offset:12288
	global_load_dwordx4 v[8:11], v[106:107], off
	global_load_dwordx4 a[176:179], v[12:13], off
	global_load_dwordx4 a[180:183], v[12:13], off offset:1024
	global_load_dwordx4 a[184:187], v[12:13], off offset:2048
	global_load_dwordx4 a[188:191], v[12:13], off offset:3072
	s_waitcnt vmcnt(37)
	ds_write_b128 v213, v[58:61] offset:13312
	global_load_dwordx4 v[12:15], v[106:107], off offset:1024
	global_load_dwordx4 a[192:195], v142, s[6:7]
	global_load_dwordx4 a[196:199], v142, s[6:7] offset:1024
	global_load_dwordx4 a[200:203], v142, s[6:7] offset:2048
	global_load_dwordx4 a[204:207], v142, s[6:7] offset:3072
	s_mov_b32 s7, 0x1f000
	v_add_co_u32_e32 v16, vcc, s7, v2
	s_waitcnt vmcnt(41)
	ds_write_b128 v213, v[62:65] offset:14336
	global_load_dwordx4 v[24:27], v[106:107], off offset:2048
	s_waitcnt vmcnt(41)
	ds_write_b128 v213, v[66:69] offset:15360
	s_waitcnt vmcnt(40)
	ds_write_b128 v213, v[70:73] offset:16384
	s_waitcnt vmcnt(39)
	ds_write_b128 v213, v[74:77] offset:17408
	s_waitcnt vmcnt(38)
	ds_write_b128 v213, v[78:81] offset:18432
	s_waitcnt vmcnt(37)
	ds_write_b128 v213, v[82:85] offset:19456
	s_waitcnt vmcnt(36)
	ds_write_b128 v213, v[86:89] offset:20480
	s_waitcnt vmcnt(35)
	ds_write_b128 v213, v[90:93] offset:21504
	s_waitcnt vmcnt(34)
	ds_write_b128 v213, v[94:97] offset:22528
	v_addc_co_u32_e32 v17, vcc, 0, v3, vcc
	global_load_dwordx4 v[28:31], v[106:107], off offset:3072
	global_load_dwordx4 v[36:39], v[16:17], off
	global_load_dwordx4 v[40:43], v[16:17], off offset:1024
	global_load_dwordx4 v[48:51], v[16:17], off offset:2048
	global_load_dwordx4 v[52:55], v[16:17], off offset:3072
	v_lshl_add_u64 v[16:17], s[4:5], 0, v[144:145]
	v_lshl_add_u64 v[16:17], v[16:17], 0, s[0:1]
	v_and_b32_e32 v142, 48, v0
	v_lshl_add_u64 v[18:19], v[16:17], 0, v[142:143]
	global_load_dwordx4 v[56:59], v[18:19], off
	s_mov_b32 s1, 0xe000
	v_add_co_u32_e32 v16, vcc, s1, v2
	s_mov_b32 s6, 0xd000
	s_nop 0
	v_addc_co_u32_e32 v17, vcc, 0, v3, vcc
	v_add_co_u32_e32 v20, vcc, s6, v2
	s_mov_b32 s1, 0xf000
	s_nop 0
	v_addc_co_u32_e32 v21, vcc, 0, v3, vcc
	global_load_dwordx4 a[208:211], v[16:17], off offset:-4096
	global_load_dwordx4 a[212:215], v[16:17], off
	global_load_dwordx4 a[216:219], v[16:17], off offset:1024
	global_load_dwordx4 a[220:223], v[16:17], off offset:2048
	global_load_dwordx4 a[224:227], v[20:21], off offset:1024
	global_load_dwordx4 a[228:231], v[20:21], off offset:2048
	v_lshlrev_b32_e32 v143, 10, v32
	v_or_b32_e32 v144, v144, v142
	s_waitcnt vmcnt(31)
	ds_write_b128 v213, v[4:7] offset:23552
	v_add_co_u32_e32 v6, vcc, s1, v2
	s_mov_b32 s1, 0x10000
	s_nop 0
	v_addc_co_u32_e32 v7, vcc, 0, v3, vcc
	v_add_co_u32_e32 v22, vcc, s1, v2
	s_mov_b32 s1, 0x11000
	s_nop 0
	v_addc_co_u32_e32 v23, vcc, 0, v3, vcc
	global_load_dwordx4 a[232:235], v[16:17], off offset:3072
	global_load_dwordx4 a[236:239], v[22:23], off offset:-4096
	global_load_dwordx4 a[240:243], v[20:21], off offset:3072
	global_load_dwordx4 a[244:247], v[6:7], off offset:1024
	s_waitcnt vmcnt(26)
	ds_write_b128 v213, v[8:11] offset:24576
	s_waitcnt vmcnt(21)
	ds_write_b128 v213, v[12:15] offset:25600
	global_load_dwordx4 v[10:13], v[18:19], off offset:64
	v_add_co_u32_e32 v34, vcc, s1, v2
	s_mov_b32 s1, 0x12000
	s_nop 0
	v_addc_co_u32_e32 v35, vcc, 0, v3, vcc
	v_add_co_u32_e32 v66, vcc, s1, v2
	s_mov_b32 s1, 0x13000
	s_nop 0
	v_addc_co_u32_e32 v67, vcc, 0, v3, vcc
	v_add_co_u32_e32 v46, vcc, s1, v2
	s_mov_b32 s1, 0x14000
	s_nop 0
	v_addc_co_u32_e32 v47, vcc, 0, v3, vcc
	v_add_co_u32_e32 v86, vcc, s1, v2
	s_mov_b32 s1, 0x15000
	s_nop 0
	v_addc_co_u32_e32 v87, vcc, 0, v3, vcc
	v_add_co_u32_e32 v122, vcc, s1, v2
	s_mov_b32 s1, 0x16000
	s_nop 0
	v_addc_co_u32_e32 v123, vcc, 0, v3, vcc
	v_lshrrev_b32_e32 v14, 1, v0
	v_add_co_u32_e32 v106, vcc, s1, v2
	v_and_or_b32 v152, v14, 8, v143
	s_waitcnt vmcnt(11)
	v_cvt_f32_f16_e32 v14, v56
	v_addc_co_u32_e32 v107, vcc, 0, v3, vcc
	s_mov_b32 s1, 0x17000
	ds_write_b128 v213, v[24:27] offset:26624
	ds_write_b128 v213, v[28:31] offset:27648
	v_add_co_u32_e32 v134, vcc, s1, v2
	ds_write_b128 v213, v[36:39] offset:28672
	s_nop 0
	v_addc_co_u32_e32 v135, vcc, 0, v3, vcc
	global_load_dwordx4 v[2:5], v[6:7], off offset:2048
	s_nop 0
	global_load_dwordx4 v[6:9], v[6:7], off offset:3072
	ds_write_b128 v213, v[40:43] offset:29696
	ds_write_b128 v213, v[48:51] offset:30720
	ds_write_b128 v213, v[52:55] offset:31744
	v_lshl_add_u32 v217, v1, 4, v152
	v_bitop3_b32 v1, v33, v32, 2 bitop3:0x36
	v_lshl_add_u32 v215, v1, 4, v152
	v_exp_f32_e32 v1, v14
	global_load_dwordx4 v[14:17], v[18:19], off offset:128
	global_load_dwordx4 v[138:141], v[18:19], off offset:192
	v_cvt_f32_f16_sdwa v20, v56 dst_sel:DWORD dst_unused:UNUSED_PAD src0_sel:WORD_1
	v_cvt_f32_f16_e32 v21, v57
	v_cvt_f32_f16_sdwa v25, v57 dst_sel:DWORD dst_unused:UNUSED_PAD src0_sel:WORD_1
	v_add_f32_e32 v1, 1.0, v1
	v_exp_f32_e32 v24, v20
	v_rcp_f32_e32 v20, v1
	v_exp_f32_e32 v1, v21
	v_exp_f32_e32 v25, v25
	v_add_f32_e32 v21, 1.0, v24
	v_rcp_f32_e32 v21, v21
	v_add_f32_e32 v1, 1.0, v1
	v_rcp_f32_e32 v24, v1
	v_add_f32_e32 v1, 1.0, v25
	v_rcp_f32_e32 v25, v1
	v_pk_fma_f32 v[20:21], v[20:21], 2.0, 1.0 op_sel_hi:[1,0,0] neg_lo:[1,0,0] neg_hi:[1,0,0]
	v_cvt_f32_f16_e32 v1, v58
	s_add_i32 s1, 0, 0x24000
	v_pk_fma_f32 v[24:25], v[24:25], 2.0, 1.0 op_sel_hi:[1,0,0] neg_lo:[1,0,0] neg_hi:[1,0,0]
	v_cvt_pk_f16_f32 v20, v20, v21
	v_cvt_pk_f16_f32 v21, v24, v25
	v_add_u32_e32 v24, s1, v217
	ds_write_b64 v24, v[20:21]
	v_cvt_f32_f16_sdwa v20, v58 dst_sel:DWORD dst_unused:UNUSED_PAD src0_sel:WORD_1
	v_exp_f32_e32 v1, v1
	v_cvt_f32_f16_e32 v21, v59
	v_cvt_f32_f16_sdwa v24, v59 dst_sel:DWORD dst_unused:UNUSED_PAD src0_sel:WORD_1
	v_exp_f32_e32 v25, v20
	v_add_f32_e32 v1, 1.0, v1
	v_rcp_f32_e32 v20, v1
	v_exp_f32_e32 v1, v21
	v_add_f32_e32 v21, 1.0, v25
	v_exp_f32_e32 v25, v24
	v_rcp_f32_e32 v21, v21
	v_add_f32_e32 v1, 1.0, v1
	v_rcp_f32_e32 v24, v1
	v_add_f32_e32 v1, 1.0, v25
	v_rcp_f32_e32 v25, v1
	s_waitcnt vmcnt(4)
	v_cvt_f32_f16_e32 v1, v10
	v_cvt_f32_f16_sdwa v10, v10 dst_sel:DWORD dst_unused:UNUSED_PAD src0_sel:WORD_1
	v_pk_fma_f32 v[20:21], v[20:21], 2.0, 1.0 op_sel_hi:[1,0,0] neg_lo:[1,0,0] neg_hi:[1,0,0]
	v_pk_fma_f32 v[24:25], v[24:25], 2.0, 1.0 op_sel_hi:[1,0,0] neg_lo:[1,0,0] neg_hi:[1,0,0]
	v_cvt_pk_f16_f32 v20, v20, v21
	v_cvt_pk_f16_f32 v21, v24, v25
	v_exp_f32_e32 v1, v1
	v_add_u32_e32 v24, s1, v215
	ds_write_b64 v24, v[20:21]
	v_cvt_f32_f16_e32 v20, v11
	v_exp_f32_e32 v21, v10
	v_cvt_f32_f16_sdwa v11, v11 dst_sel:DWORD dst_unused:UNUSED_PAD src0_sel:WORD_1
	v_add_f32_e32 v1, 1.0, v1
	v_rcp_f32_e32 v10, v1
	v_exp_f32_e32 v1, v20
	v_add_f32_e32 v20, 1.0, v21
	v_exp_f32_e32 v21, v11
	v_rcp_f32_e32 v11, v20
	v_add_f32_e32 v1, 1.0, v1
	v_rcp_f32_e32 v20, v1
	v_add_f32_e32 v1, 1.0, v21
	v_rcp_f32_e32 v21, v1
	v_bitop3_b32 v26, v33, v32, 4 bitop3:0x36
	v_bitop3_b32 v1, v33, v32, 6 bitop3:0x36
	v_lshl_add_u32 v211, v26, 4, v152
	v_lshl_add_u32 v212, v1, 4, v152
	v_pk_fma_f32 v[10:11], v[10:11], 2.0, 1.0 op_sel_hi:[1,0,0] neg_lo:[1,0,0] neg_hi:[1,0,0]
	v_pk_fma_f32 v[20:21], v[20:21], 2.0, 1.0 op_sel_hi:[1,0,0] neg_lo:[1,0,0] neg_hi:[1,0,0]
	v_bitop3_b32 v1, v33, v32, 8 bitop3:0x36
	v_cvt_pk_f16_f32 v10, v10, v11
	v_cvt_pk_f16_f32 v11, v20, v21
	v_lshl_add_u32 v210, v1, 4, v152
	v_add_u32_e32 v1, s1, v211
	ds_write_b64 v1, v[10:11]
	v_cvt_f32_f16_e32 v10, v12
	v_cvt_f32_f16_sdwa v11, v12 dst_sel:DWORD dst_unused:UNUSED_PAD src0_sel:WORD_1
	v_cvt_f32_f16_e32 v12, v13
	v_cvt_f32_f16_sdwa v13, v13 dst_sel:DWORD dst_unused:UNUSED_PAD src0_sel:WORD_1
	v_exp_f32_e32 v10, v10
	v_exp_f32_e32 v11, v11
	v_exp_f32_e32 v12, v12
	v_exp_f32_e32 v13, v13
	v_add_f32_e32 v10, 1.0, v10
	v_add_f32_e32 v11, 1.0, v11
	v_add_f32_e32 v12, 1.0, v12
	v_add_f32_e32 v13, 1.0, v13
	v_rcp_f32_e32 v10, v10
	v_rcp_f32_e32 v11, v11
	v_rcp_f32_e32 v12, v12
	v_rcp_f32_e32 v13, v13
	s_waitcnt vmcnt(1)
	v_cvt_f32_f16_e32 v20, v14
	v_pk_fma_f32 v[10:11], v[10:11], 2.0, 1.0 op_sel_hi:[1,0,0] neg_lo:[1,0,0] neg_hi:[1,0,0]
	v_cvt_f32_f16_sdwa v14, v14 dst_sel:DWORD dst_unused:UNUSED_PAD src0_sel:WORD_1
	v_pk_fma_f32 v[12:13], v[12:13], 2.0, 1.0 op_sel_hi:[1,0,0] neg_lo:[1,0,0] neg_hi:[1,0,0]
	v_cvt_pk_f16_f32 v10, v10, v11
	v_cvt_pk_f16_f32 v11, v12, v13
	v_add_u32_e32 v13, s1, v212
	v_exp_f32_e32 v12, v20
	ds_write_b64 v13, v[10:11]
	v_cvt_f32_f16_e32 v11, v15
	v_cvt_f32_f16_sdwa v13, v15 dst_sel:DWORD dst_unused:UNUSED_PAD src0_sel:WORD_1
	v_add_f32_e32 v10, 1.0, v12
	v_exp_f32_e32 v12, v14
	v_exp_f32_e32 v14, v11
	v_exp_f32_e32 v13, v13
	v_rcp_f32_e32 v10, v10
	v_add_f32_e32 v11, 1.0, v12
	v_add_f32_e32 v12, 1.0, v14
	v_add_f32_e32 v13, 1.0, v13
	v_rcp_f32_e32 v11, v11
	v_rcp_f32_e32 v12, v12
	v_rcp_f32_e32 v13, v13
	v_cvt_f32_f16_e32 v14, v16
	v_pk_fma_f32 v[10:11], v[10:11], 2.0, 1.0 op_sel_hi:[1,0,0] neg_lo:[1,0,0] neg_hi:[1,0,0]
	v_add_co_u32_e32 v150, vcc, s2, v18
	v_pk_fma_f32 v[12:13], v[12:13], 2.0, 1.0 op_sel_hi:[1,0,0] neg_lo:[1,0,0] neg_hi:[1,0,0]
	v_cvt_pk_f16_f32 v10, v10, v11
	v_cvt_pk_f16_f32 v11, v12, v13
	v_exp_f32_e32 v12, v14
	v_cvt_f32_f16_sdwa v14, v16 dst_sel:DWORD dst_unused:UNUSED_PAD src0_sel:WORD_1
	v_add_u32_e32 v13, s1, v210
	ds_write_b64 v13, v[10:11]
	v_add_f32_e32 v10, 1.0, v12
	v_cvt_f32_f16_e32 v11, v17
	v_exp_f32_e32 v12, v14
	v_cvt_f32_f16_sdwa v13, v17 dst_sel:DWORD dst_unused:UNUSED_PAD src0_sel:WORD_1
	v_rcp_f32_e32 v10, v10
	v_exp_f32_e32 v14, v11
	v_add_f32_e32 v11, 1.0, v12
	v_exp_f32_e32 v12, v13
	v_rcp_f32_e32 v11, v11
	v_add_f32_e32 v13, 1.0, v14
	v_bitop3_b32 v1, v33, v32, 10 bitop3:0x36
	v_add_f32_e32 v12, 1.0, v12
	v_rcp_f32_e32 v146, v13
	v_rcp_f32_e32 v147, v12
	v_pk_fma_f32 v[148:149], v[10:11], 2.0, 1.0 op_sel_hi:[1,0,0] neg_lo:[1,0,0] neg_hi:[1,0,0]
	global_load_dwordx4 v[10:13], v[22:23], off
	global_load_dwordx4 v[14:17], v[22:23], off offset:1024
	v_addc_co_u32_e32 v151, vcc, 0, v19, vcc
	global_load_dwordx4 v[18:21], v[22:23], off offset:2048
	s_nop 0
	global_load_dwordx4 v[22:25], v[22:23], off offset:3072
	s_nop 0
	global_load_dwordx4 v[26:29], v[34:35], off offset:1024
	global_load_dwordx4 v[30:33], v[34:35], off offset:2048
	s_nop 0
	global_load_dwordx4 v[34:37], v[34:35], off offset:3072
	s_nop 0
	global_load_dwordx4 v[38:41], v[46:47], off offset:1024
	global_load_dwordx4 v[42:45], v[46:47], off offset:2048
	s_nop 0
	global_load_dwordx4 v[46:49], v[46:47], off offset:3072
	s_nop 0
	global_load_dwordx4 v[50:53], v[66:67], off offset:-4096
	global_load_dwordx4 v[54:57], v[66:67], off
	global_load_dwordx4 v[58:61], v[66:67], off offset:1024
	global_load_dwordx4 v[62:65], v[66:67], off offset:2048
	s_nop 0
	global_load_dwordx4 v[66:69], v[66:67], off offset:3072
	s_nop 0
	global_load_dwordx4 v[70:73], v[86:87], off offset:-4096
	global_load_dwordx4 v[74:77], v[86:87], off
	global_load_dwordx4 v[78:81], v[86:87], off offset:1024
	global_load_dwordx4 v[82:85], v[86:87], off offset:2048
	s_nop 0
	global_load_dwordx4 v[86:89], v[86:87], off offset:3072
	s_nop 0
	global_load_dwordx4 v[90:93], v[106:107], off offset:-4096
	global_load_dwordx4 v[94:97], v[106:107], off
	global_load_dwordx4 v[98:101], v[106:107], off offset:1024
	global_load_dwordx4 v[102:105], v[106:107], off offset:2048
	s_nop 0
	global_load_dwordx4 v[106:109], v[106:107], off offset:3072
	s_nop 0
	global_load_dwordx4 v[110:113], v[110:111], off offset:-4096
	s_nop 0
	global_load_dwordx4 v[114:117], v[122:123], off offset:1024
	global_load_dwordx4 v[118:121], v[122:123], off offset:2048
	s_nop 0
	global_load_dwordx4 v[122:125], v[122:123], off offset:3072
	s_nop 0
	global_load_dwordx4 v[126:129], v[134:135], off offset:1024
	global_load_dwordx4 v[130:133], v[134:135], off offset:2048
	s_nop 0
	global_load_dwordx4 v[134:137], v[134:135], off offset:3072
	s_nop 0
	global_load_dwordx4 v[178:181], v[150:151], off
	global_load_dwordx4 v[174:177], v[150:151], off offset:64
	global_load_dwordx4 v[170:173], v[150:151], off offset:128
	global_load_dwordx4 v[202:205], v[150:151], off offset:192
	s_waitcnt vmcnt(36)
	v_cvt_f32_f16_e32 v155, v138
	v_cvt_f32_f16_sdwa v138, v138 dst_sel:DWORD dst_unused:UNUSED_PAD src0_sel:WORD_1
	v_pk_fma_f32 v[146:147], v[146:147], 2.0, 1.0 op_sel_hi:[1,0,0] neg_lo:[1,0,0] neg_hi:[1,0,0]
	v_cvt_pk_f16_f32 v148, v148, v149
	v_exp_f32_e32 v150, v155
	v_cvt_pk_f16_f32 v149, v146, v147
	v_cvt_f32_f16_e32 v147, v139
	v_cvt_f32_f16_sdwa v139, v139 dst_sel:DWORD dst_unused:UNUSED_PAD src0_sel:WORD_1
	v_add_f32_e32 v146, 1.0, v150
	v_exp_f32_e32 v150, v138
	v_rcp_f32_e32 v138, v146
	v_exp_f32_e32 v146, v147
	v_lshl_add_u32 v1, v1, 4, v152
	v_add_f32_e32 v147, 1.0, v150
	v_exp_f32_e32 v150, v139
	v_rcp_f32_e32 v139, v147
	v_add_f32_e32 v146, 1.0, v146
	v_rcp_f32_e32 v146, v146
	v_add_f32_e32 v147, 1.0, v150
	v_rcp_f32_e32 v147, v147
	v_pk_fma_f32 v[138:139], v[138:139], 2.0, 1.0 op_sel_hi:[1,0,0] neg_lo:[1,0,0] neg_hi:[1,0,0]
	v_add_u32_e32 v151, s1, v1
	v_cvt_pk_f16_f32 v138, v138, v139
	v_pk_fma_f32 v[146:147], v[146:147], 2.0, 1.0 op_sel_hi:[1,0,0] neg_lo:[1,0,0] neg_hi:[1,0,0]
	ds_write_b64 v151, v[148:149]
	v_cvt_pk_f16_f32 v139, v146, v147
	v_cvt_f32_f16_e32 v146, v140
	v_cvt_f32_f16_sdwa v140, v140 dst_sel:DWORD dst_unused:UNUSED_PAD src0_sel:WORD_1
	v_cvt_f32_f16_e32 v147, v141
	v_cvt_f32_f16_sdwa v141, v141 dst_sel:DWORD dst_unused:UNUSED_PAD src0_sel:WORD_1
	v_exp_f32_e32 v146, v146
	v_exp_f32_e32 v148, v140
	v_lshl_add_u32 v216, v153, 4, v152
	v_lshl_add_u32 v214, v154, 4, v152
	v_add_f32_e32 v140, 1.0, v146
	v_exp_f32_e32 v146, v147
	v_add_f32_e32 v147, 1.0, v148
	v_exp_f32_e32 v148, v141
	v_rcp_f32_e32 v141, v147
	v_add_f32_e32 v146, 1.0, v146
	v_rcp_f32_e32 v140, v140
	v_add_f32_e32 v147, 1.0, v148
	v_rcp_f32_e32 v146, v146
	v_rcp_f32_e32 v147, v147
	v_add_u32_e32 v148, s1, v216
	ds_write_b64 v148, v[138:139]
	v_pk_fma_f32 v[138:139], v[140:141], 2.0, 1.0 op_sel_hi:[1,0,0] neg_lo:[1,0,0] neg_hi:[1,0,0]
	v_pk_fma_f32 v[140:141], v[146:147], 2.0, 1.0 op_sel_hi:[1,0,0] neg_lo:[1,0,0] neg_hi:[1,0,0]
	v_cvt_pk_f16_f32 v138, v138, v139
	v_cvt_pk_f16_f32 v139, v140, v141
	v_add_u32_e32 v140, s1, v214
	s_lshl_b32 s2, s12, 7
	s_add_i32 s1, 0, 0x20000
	s_add_u32 s0, s4, s0
	ds_write_b64 v140, v[138:139]
	v_add_u32_e32 v219, s1, v143
	v_bitop3_b32 v138, v218, v0, 15 bitop3:0x78
	s_addc_u32 s1, s5, 0
	v_lshlrev_b32_e32 v220, 4, v138
	v_lshl_add_u64 v[138:139], s[0:1], 0, v[144:145]
	s_mov_b64 s[0:1], 0x800080
	s_waitcnt lgkmcnt(0)
	s_barrier
	v_lshl_add_u64 v[208:209], v[138:139], 0, s[0:1]
	s_waitcnt vmcnt(0)
	v_mov_b32_e32 v232, v170
	v_mov_b32_e32 v233, v171
	v_mov_b32_e32 v234, v172
	v_mov_b32_e32 v235, v173
	v_mov_b32_e32 v236, v202
	v_mov_b32_e32 v237, v203
	v_mov_b32_e32 v238, v204
	v_mov_b32_e32 v239, v205
	v_cvt_f32_f16_e32 v198, v178
	v_cvt_f32_f16_sdwa v199, v178 dst_sel:DWORD dst_unused:UNUSED_PAD src0_sel:WORD_1
	v_cvt_f32_f16_e32 v200, v179
	v_cvt_f32_f16_sdwa v201, v179 dst_sel:DWORD dst_unused:UNUSED_PAD src0_sel:WORD_1
	v_cvt_f32_f16_e32 v194, v180
	v_cvt_f32_f16_sdwa v195, v180 dst_sel:DWORD dst_unused:UNUSED_PAD src0_sel:WORD_1
	v_cvt_f32_f16_e32 v196, v181
	v_cvt_f32_f16_sdwa v197, v181 dst_sel:DWORD dst_unused:UNUSED_PAD src0_sel:WORD_1
	v_cvt_f32_f16_e32 v190, v174
	v_cvt_f32_f16_sdwa v191, v174 dst_sel:DWORD dst_unused:UNUSED_PAD src0_sel:WORD_1
	v_cvt_f32_f16_e32 v192, v175
	v_cvt_f32_f16_sdwa v193, v175 dst_sel:DWORD dst_unused:UNUSED_PAD src0_sel:WORD_1
	v_cvt_f32_f16_e32 v186, v176
	v_cvt_f32_f16_sdwa v187, v176 dst_sel:DWORD dst_unused:UNUSED_PAD src0_sel:WORD_1
	v_cvt_f32_f16_e32 v188, v177
	v_cvt_f32_f16_sdwa v189, v177 dst_sel:DWORD dst_unused:UNUSED_PAD src0_sel:WORD_1
	s_mov_b64 s[0:1], 0x400000
	v_xor_b32_e32 v221, 64, v220
	v_xor_b32_e32 v222, 0x80, v220
	v_xor_b32_e32 v223, 0xc0, v220
	ds_read_b128 v[154:157], v213 offset:0
	ds_read_b128 v[158:161], v213 offset:1024
	ds_read_b128 v[162:165], v213 offset:2048
	ds_read_b128 v[166:169], v213 offset:3072
	s_waitcnt lgkmcnt(0)
.Lrnn_top:
	s_add_i32 s4, s3, 0xffffc000
	s_and_b32 s4, s4, 0x4000
	s_and_b32 s5, s3, 0x4000
	s_add_i32 s5, s5, 0x20000
	v_add_u32_e32 v244, s4, v219
	v_add_u32_e32 v240, v244, v220
	v_add_u32_e32 v241, v244, v221
	v_add_u32_e32 v242, v244, v222
	v_add_u32_e32 v243, v244, v223
	ds_read_b128 v[138:141], v240 offset:0
	ds_read_b128 v[142:145], v241 offset:0
	ds_read_b128 v[146:149], v240 offset:256
	ds_read_b128 v[150:153], v240 offset:768
	s_cmp_eq_u32 s3, 0x40000
	s_cbranch_scc1 .Lrnn_sk1
	global_load_dwordx4 v[224:227], v[208:209], off offset:-128
	global_load_dwordx4 v[228:231], v[208:209], off offset:-64
.Lrnn_sk1:
	s_waitcnt lgkmcnt(3)
	v_mfma_f32_16x16x32_f16 v[198:201], a[192:195], v[138:141], v[198:201]
	v_mfma_f32_16x16x32_f16 v[194:197], a[196:199], v[138:141], v[194:197]
	s_waitcnt vmcnt(2)
	v_cvt_f32_f16_e32 v182, v232
	v_mfma_f32_16x16x32_f16 v[190:193], a[200:203], v[138:141], v[190:193]
	v_cvt_f32_f16_sdwa v183, v232 dst_sel:DWORD dst_unused:UNUSED_PAD src0_sel:WORD_1
	v_cvt_f32_f16_e32 v184, v233
	v_mfma_f32_16x16x32_f16 v[186:189], a[204:207], v[138:141], v[186:189]
	ds_read_b128 v[138:141], v241 offset:256
	v_cvt_f32_f16_sdwa v185, v233 dst_sel:DWORD dst_unused:UNUSED_PAD src0_sel:WORD_1
	v_cvt_f32_f16_e32 v178, v234
	s_waitcnt lgkmcnt(3)
	v_mfma_f32_16x16x32_f16 v[198:201], a[12:15], v[142:145], v[198:201]
	v_cvt_f32_f16_sdwa v179, v234 dst_sel:DWORD dst_unused:UNUSED_PAD src0_sel:WORD_1
	v_cvt_f32_f16_e32 v180, v235
	v_mfma_f32_16x16x32_f16 v[194:197], a[16:19], v[142:145], v[194:197]
	v_cvt_f32_f16_sdwa v181, v235 dst_sel:DWORD dst_unused:UNUSED_PAD src0_sel:WORD_1
	v_cvt_f32_f16_e32 v174, v236
	v_mfma_f32_16x16x32_f16 v[190:193], a[20:23], v[142:145], v[190:193]
	v_cvt_f32_f16_sdwa v175, v236 dst_sel:DWORD dst_unused:UNUSED_PAD src0_sel:WORD_1
	v_cvt_f32_f16_e32 v176, v237
	v_mfma_f32_16x16x32_f16 v[186:189], a[24:27], v[142:145], v[186:189]
	ds_read_b128 v[142:145], v240 offset:512
	v_cvt_f32_f16_sdwa v177, v237 dst_sel:DWORD dst_unused:UNUSED_PAD src0_sel:WORD_1
	v_cvt_f32_f16_e32 v170, v238
	s_waitcnt lgkmcnt(3)
	v_mfma_f32_16x16x32_f16 v[198:201], a[112:115], v[146:149], v[198:201]
	v_cvt_f32_f16_sdwa v171, v238 dst_sel:DWORD dst_unused:UNUSED_PAD src0_sel:WORD_1
	v_cvt_f32_f16_e32 v172, v239
	v_mfma_f32_16x16x32_f16 v[194:197], a[116:119], v[146:149], v[194:197]
	v_cvt_f32_f16_sdwa v173, v239 dst_sel:DWORD dst_unused:UNUSED_PAD src0_sel:WORD_1
	v_mfma_f32_16x16x32_f16 v[190:193], a[120:123], v[146:149], v[190:193]
	s_cmp_eq_u32 s3, 0x40000
	s_cbranch_scc1 .Lrnn_sk2
	global_load_dwordx4 v[232:235], v[208:209], off
	global_load_dwordx4 v[236:239], v[208:209], off offset:64
.Lrnn_sk2:
	v_mfma_f32_16x16x32_f16 v[186:189], a[124:127], v[146:149], v[186:189]
	ds_read_b128 v[146:149], v241 offset:512
	s_waitcnt lgkmcnt(3)
	v_mfma_f32_16x16x32_f16 v[198:201], v[154:157], v[150:153], v[198:201]
	ds_read_b128 v[154:157], v213 offset:8192
	v_mfma_f32_16x16x32_f16 v[194:197], v[158:161], v[150:153], v[194:197]
	ds_read_b128 v[158:161], v213 offset:9216
	v_mfma_f32_16x16x32_f16 v[190:193], v[162:165], v[150:153], v[190:193]
	ds_read_b128 v[162:165], v213 offset:10240
	v_mfma_f32_16x16x32_f16 v[186:189], v[166:169], v[150:153], v[186:189]
	ds_read_b128 v[166:169], v213 offset:11264
	ds_read_b128 v[150:153], v241 offset:768
	s_waitcnt lgkmcnt(7)
	v_mfma_f32_16x16x32_f16 v[198:201], a[140:143], v[138:141], v[198:201]
	v_mfma_f32_16x16x32_f16 v[194:197], a[144:147], v[138:141], v[194:197]
	v_mfma_f32_16x16x32_f16 v[190:193], a[148:151], v[138:141], v[190:193]
	v_mfma_f32_16x16x32_f16 v[186:189], a[168:171], v[138:141], v[186:189]
	ds_read_b128 v[138:141], v242 offset:0
	s_waitcnt lgkmcnt(7)
	v_mfma_f32_16x16x32_f16 v[198:201], v[10:13], v[142:145], v[198:201]
	v_mfma_f32_16x16x32_f16 v[194:197], v[14:17], v[142:145], v[194:197]
	v_mfma_f32_16x16x32_f16 v[190:193], v[18:21], v[142:145], v[190:193]
	v_mfma_f32_16x16x32_f16 v[186:189], v[22:25], v[142:145], v[186:189]
	ds_read_b128 v[142:145], v243 offset:0
	s_waitcnt lgkmcnt(7)
	v_mfma_f32_16x16x32_f16 v[198:201], v[54:57], v[146:149], v[198:201]
	v_mfma_f32_16x16x32_f16 v[194:197], v[58:61], v[146:149], v[194:197]
	v_mfma_f32_16x16x32_f16 v[190:193], v[62:65], v[146:149], v[190:193]
	v_mfma_f32_16x16x32_f16 v[186:189], v[66:69], v[146:149], v[186:189]
	ds_read_b128 v[146:149], v242 offset:256
	s_waitcnt lgkmcnt(3)
	v_mfma_f32_16x16x32_f16 v[198:201], v[154:157], v[150:153], v[198:201]
	ds_read_b128 v[154:157], v213 offset:16384
	v_mfma_f32_16x16x32_f16 v[194:197], v[158:161], v[150:153], v[194:197]
	ds_read_b128 v[158:161], v213 offset:17408
	v_mfma_f32_16x16x32_f16 v[190:193], v[162:165], v[150:153], v[190:193]
	ds_read_b128 v[162:165], v213 offset:18432
	v_mfma_f32_16x16x32_f16 v[186:189], v[166:169], v[150:153], v[186:189]
	ds_read_b128 v[166:169], v213 offset:19456
	ds_read_b128 v[150:153], v242 offset:768
	s_waitcnt lgkmcnt(7)
	v_mfma_f32_16x16x32_f16 v[198:201], a[48:51], v[138:141], v[198:201]
	v_mfma_f32_16x16x32_f16 v[194:197], a[52:55], v[138:141], v[194:197]
	v_mfma_f32_16x16x32_f16 v[190:193], a[56:59], v[138:141], v[190:193]
	v_mfma_f32_16x16x32_f16 v[186:189], a[60:63], v[138:141], v[186:189]
	ds_read_b128 v[138:141], v243 offset:256
	s_waitcnt lgkmcnt(7)
	v_mfma_f32_16x16x32_f16 v[198:201], a[76:79], v[142:145], v[198:201]
	v_mfma_f32_16x16x32_f16 v[194:197], a[80:83], v[142:145], v[194:197]
	v_mfma_f32_16x16x32_f16 v[190:193], a[84:87], v[142:145], v[190:193]
	v_mfma_f32_16x16x32_f16 v[186:189], a[88:91], v[142:145], v[186:189]
	ds_read_b128 v[142:145], v242 offset:512
	s_waitcnt lgkmcnt(7)
	v_mfma_f32_16x16x32_f16 v[198:201], a[176:179], v[146:149], v[198:201]
	v_mfma_f32_16x16x32_f16 v[194:197], a[180:183], v[146:149], v[194:197]
	v_mfma_f32_16x16x32_f16 v[190:193], a[184:187], v[146:149], v[190:193]
	v_mfma_f32_16x16x32_f16 v[186:189], a[188:191], v[146:149], v[186:189]
	ds_read_b128 v[146:149], v243 offset:512
	s_waitcnt lgkmcnt(3)
	v_mfma_f32_16x16x32_f16 v[198:201], v[154:157], v[150:153], v[198:201]
	ds_read_b128 v[154:157], v213 offset:24576
	v_mfma_f32_16x16x32_f16 v[194:197], v[158:161], v[150:153], v[194:197]
	ds_read_b128 v[158:161], v213 offset:25600
	v_mfma_f32_16x16x32_f16 v[190:193], v[162:165], v[150:153], v[190:193]
	ds_read_b128 v[162:165], v213 offset:26624
	v_mfma_f32_16x16x32_f16 v[186:189], v[166:169], v[150:153], v[186:189]
	ds_read_b128 v[166:169], v213 offset:27648
	ds_read_b128 v[150:153], v243 offset:768
	s_waitcnt lgkmcnt(7)
	v_mfma_f32_16x16x32_f16 v[198:201], a[212:215], v[138:141], v[198:201]
	v_mfma_f32_16x16x32_f16 v[194:197], a[216:219], v[138:141], v[194:197]
	v_mfma_f32_16x16x32_f16 v[190:193], a[220:223], v[138:141], v[190:193]
	v_mfma_f32_16x16x32_f16 v[186:189], a[232:235], v[138:141], v[186:189]
	ds_read_b128 v[138:141], v240 offset:0
	s_waitcnt lgkmcnt(7)
	v_mfma_f32_16x16x32_f16 v[198:201], v[74:77], v[142:145], v[198:201]
	v_mfma_f32_16x16x32_f16 v[194:197], v[78:81], v[142:145], v[194:197]
	v_mfma_f32_16x16x32_f16 v[190:193], v[82:85], v[142:145], v[190:193]
	v_mfma_f32_16x16x32_f16 v[186:189], v[86:89], v[142:145], v[186:189]
	ds_read_b128 v[142:145], v241 offset:0
	s_waitcnt lgkmcnt(7)
	v_mfma_f32_16x16x32_f16 v[198:201], v[94:97], v[146:149], v[198:201]
	v_mfma_f32_16x16x32_f16 v[194:197], v[98:101], v[146:149], v[194:197]
	v_mfma_f32_16x16x32_f16 v[190:193], v[102:105], v[146:149], v[190:193]
	v_mfma_f32_16x16x32_f16 v[186:189], v[106:109], v[146:149], v[186:189]
	ds_read_b128 v[146:149], v240 offset:256
	s_waitcnt lgkmcnt(3)
	v_mfma_f32_16x16x32_f16 v[198:201], v[154:157], v[150:153], v[198:201]
	ds_read_b128 v[154:157], v213 offset:4096
	v_mfma_f32_16x16x32_f16 v[194:197], v[158:161], v[150:153], v[194:197]
	ds_read_b128 v[158:161], v213 offset:5120
	v_mfma_f32_16x16x32_f16 v[190:193], v[162:165], v[150:153], v[190:193]
	ds_read_b128 v[162:165], v213 offset:6144
	v_mfma_f32_16x16x32_f16 v[186:189], v[166:169], v[150:153], v[186:189]
	ds_read_b128 v[166:169], v213 offset:7168
	ds_read_b128 v[150:153], v240 offset:768
	s_waitcnt lgkmcnt(7)
	v_mfma_f32_16x16x32_f16 v[182:185], a[8:11], v[138:141], v[182:185]
	v_mfma_f32_16x16x32_f16 v[178:181], a[0:3], v[138:141], v[178:181]
	v_mfma_f32_16x16x32_f16 v[174:177], a[4:7], v[138:141], v[174:177]
	v_mfma_f32_16x16x32_f16 v[170:173], a[32:35], v[138:141], v[170:173]
	ds_read_b128 v[138:141], v241 offset:256
	s_waitcnt lgkmcnt(7)
	v_mfma_f32_16x16x32_f16 v[182:185], a[28:31], v[142:145], v[182:185]
	v_exp_f32_e32 v198, v198
	v_mfma_f32_16x16x32_f16 v[178:181], a[36:39], v[142:145], v[178:181]
	v_exp_f32_e32 v199, v199
	v_mfma_f32_16x16x32_f16 v[174:177], a[40:43], v[142:145], v[174:177]
	v_exp_f32_e32 v200, v200
	v_mfma_f32_16x16x32_f16 v[170:173], a[44:47], v[142:145], v[170:173]
	ds_read_b128 v[142:145], v240 offset:512
	v_exp_f32_e32 v201, v201
	s_waitcnt lgkmcnt(7)
	v_mfma_f32_16x16x32_f16 v[182:185], a[136:139], v[146:149], v[182:185]
	v_exp_f32_e32 v194, v194
	v_mfma_f32_16x16x32_f16 v[178:181], a[128:131], v[146:149], v[178:181]
	v_exp_f32_e32 v195, v195
	v_mfma_f32_16x16x32_f16 v[174:177], a[132:135], v[146:149], v[174:177]
	v_exp_f32_e32 v196, v196
	v_mfma_f32_16x16x32_f16 v[170:173], a[152:155], v[146:149], v[170:173]
	ds_read_b128 v[146:149], v241 offset:512
	v_exp_f32_e32 v197, v197
	s_waitcnt lgkmcnt(3)
	v_mfma_f32_16x16x32_f16 v[182:185], v[154:157], v[150:153], v[182:185]
	ds_read_b128 v[154:157], v213 offset:12288
	v_exp_f32_e32 v190, v190
	v_mfma_f32_16x16x32_f16 v[178:181], v[158:161], v[150:153], v[178:181]
	ds_read_b128 v[158:161], v213 offset:13312
	v_exp_f32_e32 v191, v191
	v_mfma_f32_16x16x32_f16 v[174:177], v[162:165], v[150:153], v[174:177]
	ds_read_b128 v[162:165], v213 offset:14336
	v_exp_f32_e32 v192, v192
	v_mfma_f32_16x16x32_f16 v[170:173], v[166:169], v[150:153], v[170:173]
	ds_read_b128 v[166:169], v213 offset:15360
	ds_read_b128 v[150:153], v241 offset:768
	v_exp_f32_e32 v193, v193
	s_waitcnt lgkmcnt(7)
	v_mfma_f32_16x16x32_f16 v[182:185], a[172:175], v[138:141], v[182:185]
	v_exp_f32_e32 v186, v186
	v_mfma_f32_16x16x32_f16 v[178:181], a[156:159], v[138:141], v[178:181]
	v_exp_f32_e32 v187, v187
	v_mfma_f32_16x16x32_f16 v[174:177], a[160:163], v[138:141], v[174:177]
	v_exp_f32_e32 v188, v188
	v_mfma_f32_16x16x32_f16 v[170:173], a[164:167], v[138:141], v[170:173]
	ds_read_b128 v[138:141], v242 offset:0
	v_exp_f32_e32 v189, v189
	s_waitcnt lgkmcnt(7)
	v_mfma_f32_16x16x32_f16 v[182:185], v[50:53], v[142:145], v[182:185]
	v_add_f32_e32 v198, 1.0, v198
	v_add_f32_e32 v199, 1.0, v199
	v_mfma_f32_16x16x32_f16 v[178:181], v[26:29], v[142:145], v[178:181]
	v_add_f32_e32 v200, 1.0, v200
	v_add_f32_e32 v201, 1.0, v201
	v_mfma_f32_16x16x32_f16 v[174:177], v[30:33], v[142:145], v[174:177]
	v_add_f32_e32 v194, 1.0, v194
	v_add_f32_e32 v195, 1.0, v195
	v_mfma_f32_16x16x32_f16 v[170:173], v[34:37], v[142:145], v[170:173]
	ds_read_b128 v[142:145], v243 offset:0
	v_add_f32_e32 v196, 1.0, v196
	v_add_f32_e32 v197, 1.0, v197
	s_waitcnt lgkmcnt(7)
	v_mfma_f32_16x16x32_f16 v[182:185], v[70:73], v[146:149], v[182:185]
	v_add_f32_e32 v190, 1.0, v190
	v_add_f32_e32 v191, 1.0, v191
	v_mfma_f32_16x16x32_f16 v[178:181], v[38:41], v[146:149], v[178:181]
	v_add_f32_e32 v192, 1.0, v192
	v_add_f32_e32 v193, 1.0, v193
	v_mfma_f32_16x16x32_f16 v[174:177], v[42:45], v[146:149], v[174:177]
	v_add_f32_e32 v186, 1.0, v186
	v_add_f32_e32 v187, 1.0, v187
	v_mfma_f32_16x16x32_f16 v[170:173], v[46:49], v[146:149], v[170:173]
	ds_read_b128 v[146:149], v242 offset:256
	v_add_f32_e32 v188, 1.0, v188
	v_add_f32_e32 v189, 1.0, v189
	s_waitcnt lgkmcnt(3)
	v_mfma_f32_16x16x32_f16 v[182:185], v[154:157], v[150:153], v[182:185]
	ds_read_b128 v[154:157], v213 offset:20480
	v_rcp_f32_e32 v198, v198
	v_mfma_f32_16x16x32_f16 v[178:181], v[158:161], v[150:153], v[178:181]
	ds_read_b128 v[158:161], v213 offset:21504
	v_rcp_f32_e32 v199, v199
	v_mfma_f32_16x16x32_f16 v[174:177], v[162:165], v[150:153], v[174:177]
	ds_read_b128 v[162:165], v213 offset:22528
	v_rcp_f32_e32 v200, v200
	v_mfma_f32_16x16x32_f16 v[170:173], v[166:169], v[150:153], v[170:173]
	ds_read_b128 v[166:169], v213 offset:23552
	ds_read_b128 v[150:153], v242 offset:768
	v_rcp_f32_e32 v201, v201
	s_waitcnt lgkmcnt(7)
	v_mfma_f32_16x16x32_f16 v[182:185], a[72:75], v[138:141], v[182:185]
	v_rcp_f32_e32 v194, v194
	v_mfma_f32_16x16x32_f16 v[178:181], a[64:67], v[138:141], v[178:181]
	v_rcp_f32_e32 v195, v195
	v_mfma_f32_16x16x32_f16 v[174:177], a[68:71], v[138:141], v[174:177]
	v_rcp_f32_e32 v196, v196
	v_mfma_f32_16x16x32_f16 v[170:173], a[96:99], v[138:141], v[170:173]
	ds_read_b128 v[138:141], v243 offset:256
	v_rcp_f32_e32 v197, v197
	s_waitcnt lgkmcnt(7)
	v_mfma_f32_16x16x32_f16 v[182:185], a[92:95], v[142:145], v[182:185]
	v_rcp_f32_e32 v190, v190
	v_mfma_f32_16x16x32_f16 v[178:181], a[100:103], v[142:145], v[178:181]
	v_rcp_f32_e32 v191, v191
	v_mfma_f32_16x16x32_f16 v[174:177], a[104:107], v[142:145], v[174:177]
	v_rcp_f32_e32 v192, v192
	v_mfma_f32_16x16x32_f16 v[170:173], a[108:111], v[142:145], v[170:173]
	ds_read_b128 v[142:145], v242 offset:512
	v_rcp_f32_e32 v193, v193
	s_waitcnt lgkmcnt(7)
	v_mfma_f32_16x16x32_f16 v[182:185], a[208:211], v[146:149], v[182:185]
	v_rcp_f32_e32 v186, v186
	v_mfma_f32_16x16x32_f16 v[178:181], a[224:227], v[146:149], v[178:181]
	v_rcp_f32_e32 v187, v187
	v_mfma_f32_16x16x32_f16 v[174:177], a[228:231], v[146:149], v[174:177]
	v_rcp_f32_e32 v188, v188
	v_mfma_f32_16x16x32_f16 v[170:173], a[240:243], v[146:149], v[170:173]
	ds_read_b128 v[146:149], v243 offset:512
	v_rcp_f32_e32 v189, v189
	s_waitcnt lgkmcnt(3)
	v_mfma_f32_16x16x32_f16 v[182:185], v[154:157], v[150:153], v[182:185]
	ds_read_b128 v[154:157], v213 offset:28672
	v_pk_fma_f32 v[198:199], v[198:199], 2.0, 1.0 op_sel_hi:[1,0,0] neg_lo:[1,0,0] neg_hi:[1,0,0]
	v_mfma_f32_16x16x32_f16 v[178:181], v[158:161], v[150:153], v[178:181]
	ds_read_b128 v[158:161], v213 offset:29696
	v_pk_fma_f32 v[200:201], v[200:201], 2.0, 1.0 op_sel_hi:[1,0,0] neg_lo:[1,0,0] neg_hi:[1,0,0]
	v_mfma_f32_16x16x32_f16 v[174:177], v[162:165], v[150:153], v[174:177]
	ds_read_b128 v[162:165], v213 offset:30720
	v_pk_fma_f32 v[194:195], v[194:195], 2.0, 1.0 op_sel_hi:[1,0,0] neg_lo:[1,0,0] neg_hi:[1,0,0]
	v_mfma_f32_16x16x32_f16 v[170:173], v[166:169], v[150:153], v[170:173]
	ds_read_b128 v[166:169], v213 offset:31744
	ds_read_b128 v[150:153], v243 offset:768
	v_pk_fma_f32 v[196:197], v[196:197], 2.0, 1.0 op_sel_hi:[1,0,0] neg_lo:[1,0,0] neg_hi:[1,0,0]
	s_waitcnt lgkmcnt(7)
	v_mfma_f32_16x16x32_f16 v[182:185], a[236:239], v[138:141], v[182:185]
	v_pk_fma_f32 v[190:191], v[190:191], 2.0, 1.0 op_sel_hi:[1,0,0] neg_lo:[1,0,0] neg_hi:[1,0,0]
	v_mfma_f32_16x16x32_f16 v[178:181], a[244:247], v[138:141], v[178:181]
	v_pk_fma_f32 v[192:193], v[192:193], 2.0, 1.0 op_sel_hi:[1,0,0] neg_lo:[1,0,0] neg_hi:[1,0,0]
	v_mfma_f32_16x16x32_f16 v[174:177], v[2:5], v[138:141], v[174:177]
	v_pk_fma_f32 v[186:187], v[186:187], 2.0, 1.0 op_sel_hi:[1,0,0] neg_lo:[1,0,0] neg_hi:[1,0,0]
	v_mfma_f32_16x16x32_f16 v[170:173], v[6:9], v[138:141], v[170:173]
	v_pk_fma_f32 v[188:189], v[188:189], 2.0, 1.0 op_sel_hi:[1,0,0] neg_lo:[1,0,0] neg_hi:[1,0,0]
	s_waitcnt lgkmcnt(6)
	v_mfma_f32_16x16x32_f16 v[182:185], v[90:93], v[142:145], v[182:185]
	v_cvt_pk_f16_f32 v198, v198, v199
	v_cvt_pk_f16_f32 v199, v200, v201
	v_mfma_f32_16x16x32_f16 v[178:181], v[114:117], v[142:145], v[178:181]
	v_cvt_pk_f16_f32 v194, v194, v195
	v_cvt_pk_f16_f32 v195, v196, v197
	v_mfma_f32_16x16x32_f16 v[174:177], v[118:121], v[142:145], v[174:177]
	v_cvt_pk_f16_f32 v190, v190, v191
	v_cvt_pk_f16_f32 v191, v192, v193
	v_mfma_f32_16x16x32_f16 v[170:173], v[122:125], v[142:145], v[170:173]
	v_cvt_pk_f16_f32 v186, v186, v187
	v_cvt_pk_f16_f32 v187, v188, v189
	s_waitcnt lgkmcnt(5)
	v_mfma_f32_16x16x32_f16 v[182:185], v[110:113], v[146:149], v[182:185]
	v_add_u32_e32 v244, s5, v217
	v_mfma_f32_16x16x32_f16 v[178:181], v[126:129], v[146:149], v[178:181]
	ds_write_b64 v244, v[198:199]
	v_mfma_f32_16x16x32_f16 v[174:177], v[130:133], v[146:149], v[174:177]
	v_add_u32_e32 v245, s5, v215
	v_mfma_f32_16x16x32_f16 v[170:173], v[134:137], v[146:149], v[170:173]
	ds_write_b64 v245, v[194:195]
	s_waitcnt lgkmcnt(2)
	v_mfma_f32_16x16x32_f16 v[182:185], v[154:157], v[150:153], v[182:185]
	v_add_u32_e32 v246, s5, v211
	v_mfma_f32_16x16x32_f16 v[178:181], v[158:161], v[150:153], v[178:181]
	ds_write_b64 v246, v[190:191]
	v_mfma_f32_16x16x32_f16 v[174:177], v[162:165], v[150:153], v[174:177]
	v_add_u32_e32 v247, s5, v212
	v_mfma_f32_16x16x32_f16 v[170:173], v[166:169], v[150:153], v[170:173]
	ds_write_b64 v247, v[186:187]
	ds_read_b128 v[154:157], v213 offset:0
	ds_read_b128 v[158:161], v213 offset:1024
	ds_read_b128 v[162:165], v213 offset:2048
	ds_read_b128 v[166:169], v213 offset:3072
	s_waitcnt vmcnt(2)
	v_cvt_f32_f16_e32 v198, v224
	v_cvt_f32_f16_sdwa v199, v224 dst_sel:DWORD dst_unused:UNUSED_PAD src0_sel:WORD_1
	v_cvt_f32_f16_e32 v200, v225
	v_cvt_f32_f16_sdwa v201, v225 dst_sel:DWORD dst_unused:UNUSED_PAD src0_sel:WORD_1
	v_cvt_f32_f16_e32 v194, v226
	v_cvt_f32_f16_sdwa v195, v226 dst_sel:DWORD dst_unused:UNUSED_PAD src0_sel:WORD_1
	v_cvt_f32_f16_e32 v196, v227
	v_cvt_f32_f16_sdwa v197, v227 dst_sel:DWORD dst_unused:UNUSED_PAD src0_sel:WORD_1
	v_cvt_f32_f16_e32 v190, v228
	v_cvt_f32_f16_sdwa v191, v228 dst_sel:DWORD dst_unused:UNUSED_PAD src0_sel:WORD_1
	v_cvt_f32_f16_e32 v192, v229
	v_cvt_f32_f16_sdwa v193, v229 dst_sel:DWORD dst_unused:UNUSED_PAD src0_sel:WORD_1
	v_cvt_f32_f16_e32 v186, v230
	v_cvt_f32_f16_sdwa v187, v230 dst_sel:DWORD dst_unused:UNUSED_PAD src0_sel:WORD_1
	v_cvt_f32_f16_e32 v188, v231
	v_cvt_f32_f16_sdwa v189, v231 dst_sel:DWORD dst_unused:UNUSED_PAD src0_sel:WORD_1
	s_nop 7
	v_exp_f32_e32 v182, v182
	v_exp_f32_e32 v183, v183
	v_exp_f32_e32 v184, v184
	v_exp_f32_e32 v185, v185
	v_exp_f32_e32 v178, v178
	v_exp_f32_e32 v179, v179
	v_exp_f32_e32 v180, v180
	v_exp_f32_e32 v181, v181
	v_exp_f32_e32 v174, v174
	v_exp_f32_e32 v175, v175
	v_exp_f32_e32 v176, v176
	v_exp_f32_e32 v177, v177
	v_exp_f32_e32 v170, v170
	v_exp_f32_e32 v171, v171
	v_exp_f32_e32 v172, v172
	v_exp_f32_e32 v173, v173
	v_add_f32_e32 v182, 1.0, v182
	v_add_f32_e32 v183, 1.0, v183
	v_add_f32_e32 v184, 1.0, v184
	v_add_f32_e32 v185, 1.0, v185
	v_add_f32_e32 v178, 1.0, v178
	v_add_f32_e32 v179, 1.0, v179
	v_add_f32_e32 v180, 1.0, v180
	v_add_f32_e32 v181, 1.0, v181
	v_add_f32_e32 v174, 1.0, v174
	v_add_f32_e32 v175, 1.0, v175
	v_add_f32_e32 v176, 1.0, v176
	v_add_f32_e32 v177, 1.0, v177
	v_add_f32_e32 v170, 1.0, v170
	v_add_f32_e32 v171, 1.0, v171
	v_add_f32_e32 v172, 1.0, v172
	v_add_f32_e32 v173, 1.0, v173
	v_rcp_f32_e32 v182, v182
	v_rcp_f32_e32 v183, v183
	v_rcp_f32_e32 v184, v184
	v_rcp_f32_e32 v185, v185
	v_rcp_f32_e32 v178, v178
	v_rcp_f32_e32 v179, v179
	v_rcp_f32_e32 v180, v180
	v_rcp_f32_e32 v181, v181
	v_rcp_f32_e32 v174, v174
	v_rcp_f32_e32 v175, v175
	v_rcp_f32_e32 v176, v176
	v_rcp_f32_e32 v177, v177
	v_rcp_f32_e32 v170, v170
	v_rcp_f32_e32 v171, v171
	v_rcp_f32_e32 v172, v172
	v_rcp_f32_e32 v173, v173
	v_pk_fma_f32 v[182:183], v[182:183], 2.0, 1.0 op_sel_hi:[1,0,0] neg_lo:[1,0,0] neg_hi:[1,0,0]
	v_pk_fma_f32 v[184:185], v[184:185], 2.0, 1.0 op_sel_hi:[1,0,0] neg_lo:[1,0,0] neg_hi:[1,0,0]
	v_pk_fma_f32 v[178:179], v[178:179], 2.0, 1.0 op_sel_hi:[1,0,0] neg_lo:[1,0,0] neg_hi:[1,0,0]
	v_pk_fma_f32 v[180:181], v[180:181], 2.0, 1.0 op_sel_hi:[1,0,0] neg_lo:[1,0,0] neg_hi:[1,0,0]
	v_pk_fma_f32 v[174:175], v[174:175], 2.0, 1.0 op_sel_hi:[1,0,0] neg_lo:[1,0,0] neg_hi:[1,0,0]
	v_pk_fma_f32 v[176:177], v[176:177], 2.0, 1.0 op_sel_hi:[1,0,0] neg_lo:[1,0,0] neg_hi:[1,0,0]
	v_pk_fma_f32 v[170:171], v[170:171], 2.0, 1.0 op_sel_hi:[1,0,0] neg_lo:[1,0,0] neg_hi:[1,0,0]
	v_pk_fma_f32 v[172:173], v[172:173], 2.0, 1.0 op_sel_hi:[1,0,0] neg_lo:[1,0,0] neg_hi:[1,0,0]
	v_cvt_pk_f16_f32 v182, v182, v183
	v_cvt_pk_f16_f32 v183, v184, v185
	v_cvt_pk_f16_f32 v178, v178, v179
	v_cvt_pk_f16_f32 v179, v180, v181
	v_cvt_pk_f16_f32 v174, v174, v175
	v_cvt_pk_f16_f32 v175, v176, v177
	v_cvt_pk_f16_f32 v170, v170, v171
	v_cvt_pk_f16_f32 v171, v172, v173
	v_add_u32_e32 v244, s5, v210
	ds_write_b64 v244, v[182:183]
	v_add_u32_e32 v245, s5, v1
	ds_write_b64 v245, v[178:179]
	v_add_u32_e32 v246, s5, v216
	ds_write_b64 v246, v[174:175]
	v_add_u32_e32 v247, s5, v214
	ds_write_b64 v247, v[170:171]
	s_addk_i32 s3, 0x4000
	v_lshl_add_u64 v[208:209], v[208:209], 0, s[0:1]
	s_cmp_eq_u32 s3, 0x44000
	s_waitcnt lgkmcnt(0)
	s_barrier
	s_cbranch_scc0 .Lrnn_top

.LBB7_11:
	v_lshlrev_b32_e32 v0, 2, v56
	v_lshl_or_b32 v0, s13, 5, v0
	v_or_b32_e32 v26, s11, v0
	v_ashrrev_i32_e32 v27, 31, v26
	s_waitcnt lgkmcnt(0)
	v_lshl_add_u64 v[28:29], v[26:27], 2, s[4:5]
	global_load_dwordx4 v[18:21], v[28:29], off
	global_load_dwordx4 v[22:25], v[28:29], off offset:64
	s_load_dword s4, s[0:1], 0x28
	s_lshl_b32 s0, s12, 5
	s_add_i32 s0, s0, s10
	v_or_b32_e32 v28, s0, v1
	v_or_b32_e32 v29, 16, v28
	v_lshl_add_u64 v[0:1], v[26:27], 1, s[2:3]
	s_waitcnt lgkmcnt(0)
	v_mad_i64_i32 v[26:27], s[0:1], v28, s4, 0
	v_mad_i64_i32 v[28:29], s[0:1], v29, s4, 0
	v_lshl_add_u64 v[26:27], v[26:27], 1, v[0:1]
	v_lshl_add_u64 v[0:1], v[28:29], 1, v[0:1]
	s_waitcnt vmcnt(0)
	v_pk_add_f32 v[12:13], v[20:21], v[12:13]
	v_pk_add_f32 v[10:11], v[18:19], v[10:11]
	v_pk_add_f32 v[16:17], v[20:21], v[16:17]
	v_pk_add_f32 v[14:15], v[18:19], v[14:15]
	v_pk_add_f32 v[8:9], v[24:25], v[8:9]
	v_pk_add_f32 v[6:7], v[22:23], v[6:7]
	v_pk_add_f32 v[4:5], v[24:25], v[4:5]
	v_pk_add_f32 v[2:3], v[22:23], v[2:3]
	v_cvt_pk_f16_f32 v13, v12, v13
	v_cvt_pk_f16_f32 v12, v10, v11
	v_cvt_pk_f16_f32 v11, v16, v17
	v_cvt_pk_f16_f32 v10, v14, v15
	v_cvt_pk_f16_f32 v9, v8, v9
	v_cvt_pk_f16_f32 v8, v6, v7
	v_cvt_pk_f16_f32 v5, v4, v5
	v_cvt_pk_f16_f32 v4, v2, v3
	global_store_dwordx2 v[26:27], v[12:13], off
	global_store_dwordx2 v[0:1], v[10:11], off
	global_store_dwordx2 v[26:27], v[8:9], off offset:32
	global_store_dwordx2 v[0:1], v[4:5], off offset:32
	s_endpgm
	.p2align	8

.LBB8_50:
	s_endpgm
	.p2align	8

.LBB9_11:
	v_lshlrev_b32_e32 v0, 2, v90
	v_lshl_or_b32 v0, s13, 5, v0
	v_or_b32_e32 v42, s12, v0
	v_ashrrev_i32_e32 v43, 31, v42
	s_waitcnt lgkmcnt(0)
	v_lshl_add_u64 v[44:45], v[42:43], 2, s[4:5]
	global_load_dwordx4 v[34:37], v[44:45], off
	global_load_dwordx4 v[38:41], v[44:45], off offset:64
	s_load_dword s4, s[0:1], 0x28
	s_lshl_b32 s0, s11, 6
	s_add_i32 s10, s10, s0
	v_or_b32_e32 v44, s10, v1
	v_or_b32_e32 v45, 16, v44
	v_or_b32_e32 v46, 32, v44
	v_or_b32_e32 v48, 48, v44
	v_lshl_add_u64 v[0:1], v[42:43], 1, s[2:3]
	s_waitcnt lgkmcnt(0)
	v_mad_i64_i32 v[42:43], s[0:1], v44, s4, 0
	v_mad_i64_i32 v[44:45], s[0:1], v45, s4, 0
	v_mad_i64_i32 v[46:47], s[0:1], v46, s4, 0
	v_mad_i64_i32 v[48:49], s[0:1], v48, s4, 0
	v_lshl_add_u64 v[42:43], v[42:43], 1, v[0:1]
	v_lshl_add_u64 v[44:45], v[44:45], 1, v[0:1]
	v_lshl_add_u64 v[46:47], v[46:47], 1, v[0:1]
	v_lshl_add_u64 v[0:1], v[48:49], 1, v[0:1]
	s_waitcnt vmcnt(0)
	v_pk_add_f32 v[20:21], v[36:37], v[20:21]
	v_pk_add_f32 v[18:19], v[34:35], v[18:19]
	v_pk_add_f32 v[32:33], v[36:37], v[32:33]
	v_pk_add_f32 v[30:31], v[34:35], v[30:31]
	v_pk_add_f32 v[28:29], v[36:37], v[28:29]
	v_pk_add_f32 v[26:27], v[34:35], v[26:27]
	v_pk_add_f32 v[24:25], v[36:37], v[24:25]
	v_pk_add_f32 v[22:23], v[34:35], v[22:23]
	v_pk_add_f32 v[16:17], v[40:41], v[16:17]
	v_pk_add_f32 v[14:15], v[38:39], v[14:15]
	v_pk_add_f32 v[12:13], v[40:41], v[12:13]
	v_pk_add_f32 v[10:11], v[38:39], v[10:11]
	v_pk_add_f32 v[8:9], v[40:41], v[8:9]
	v_pk_add_f32 v[6:7], v[38:39], v[6:7]
	v_max_f32_e32 v18, 0, v18
	v_max_f32_e32 v19, 0, v19
	v_max_f32_e32 v20, 0, v20
	v_max_f32_e32 v21, 0, v21
	v_max_f32_e32 v30, 0, v30
	v_max_f32_e32 v31, 0, v31
	v_max_f32_e32 v32, 0, v32
	v_max_f32_e32 v33, 0, v33
	v_max_f32_e32 v26, 0, v26
	v_max_f32_e32 v27, 0, v27
	v_max_f32_e32 v28, 0, v28
	v_max_f32_e32 v29, 0, v29
	v_max_f32_e32 v22, 0, v22
	v_max_f32_e32 v23, 0, v23
	v_max_f32_e32 v24, 0, v24
	v_max_f32_e32 v25, 0, v25
	v_max_f32_e32 v14, 0, v14
	v_max_f32_e32 v34, 0, v15
	v_max_f32_e32 v15, 0, v16
	v_max_f32_e32 v16, 0, v17
	v_max_f32_e32 v35, 0, v10
	v_max_f32_e32 v36, 0, v11
	v_max_f32_e32 v17, 0, v12
	v_max_f32_e32 v37, 0, v13
	v_max_f32_e32 v48, 0, v6
	v_max_f32_e32 v49, 0, v7
	v_max_f32_e32 v50, 0, v8
	v_max_f32_e32 v51, 0, v9
	v_cvt_pk_f16_f32 v7, v20, v21
	v_cvt_pk_f16_f32 v6, v18, v19
	v_pk_add_f32 v[4:5], v[40:41], v[4:5]
	v_pk_add_f32 v[2:3], v[38:39], v[2:3]
	v_cvt_pk_f16_f32 v9, v32, v33
	v_cvt_pk_f16_f32 v8, v30, v31
	v_cvt_pk_f16_f32 v11, v28, v29
	v_cvt_pk_f16_f32 v10, v26, v27
	v_cvt_pk_f16_f32 v13, v24, v25
	v_cvt_pk_f16_f32 v12, v22, v23
	v_cvt_pk_f16_f32 v15, v15, v16
	v_cvt_pk_f16_f32 v14, v14, v34
	v_cvt_pk_f16_f32 v17, v17, v37
	v_cvt_pk_f16_f32 v16, v35, v36
	v_cvt_pk_f16_f32 v19, v50, v51
	v_cvt_pk_f16_f32 v18, v48, v49
	global_store_dwordx2 v[42:43], v[6:7], off
	global_store_dwordx2 v[44:45], v[8:9], off
	global_store_dwordx2 v[46:47], v[10:11], off
	global_store_dwordx2 v[0:1], v[12:13], off
	global_store_dwordx2 v[42:43], v[14:15], off offset:32
	global_store_dwordx2 v[44:45], v[16:17], off offset:32
	global_store_dwordx2 v[46:47], v[18:19], off offset:32
	v_max_f32_e32 v2, 0, v2
	v_max_f32_e32 v6, 0, v3
	v_max_f32_e32 v3, 0, v4
	v_max_f32_e32 v4, 0, v5
	v_cvt_pk_f16_f32 v3, v3, v4
	v_cvt_pk_f16_f32 v2, v2, v6
	global_store_dwordx2 v[0:1], v[2:3], off offset:32
	s_endpgm
	.p2align	8

.LBB10_11:
	v_lshlrev_b32_e32 v0, 2, v56
	v_lshl_or_b32 v0, s13, 5, v0
	v_or_b32_e32 v26, s11, v0
	v_ashrrev_i32_e32 v27, 31, v26
	s_waitcnt lgkmcnt(0)
	v_lshl_add_u64 v[28:29], v[26:27], 2, s[4:5]
	global_load_dwordx4 v[18:21], v[28:29], off
	global_load_dwordx4 v[22:25], v[28:29], off offset:64
	s_load_dword s4, s[0:1], 0x28
	s_lshl_b32 s0, s12, 5
	s_add_i32 s0, s0, s10
	v_or_b32_e32 v28, s0, v1
	v_or_b32_e32 v29, 16, v28
	v_lshl_add_u64 v[0:1], v[26:27], 1, s[2:3]
	s_waitcnt lgkmcnt(0)
	v_mad_i64_i32 v[26:27], s[0:1], v28, s4, 0
	v_mad_i64_i32 v[28:29], s[0:1], v29, s4, 0
	v_lshl_add_u64 v[26:27], v[26:27], 1, v[0:1]
	v_lshl_add_u64 v[0:1], v[28:29], 1, v[0:1]
	s_waitcnt vmcnt(0)
	v_pk_add_f32 v[12:13], v[20:21], v[12:13]
	v_pk_add_f32 v[10:11], v[18:19], v[10:11]
	v_pk_add_f32 v[16:17], v[20:21], v[16:17]
	v_pk_add_f32 v[14:15], v[18:19], v[14:15]
	v_pk_add_f32 v[8:9], v[24:25], v[8:9]
	v_pk_add_f32 v[6:7], v[22:23], v[6:7]
	v_pk_add_f32 v[4:5], v[24:25], v[4:5]
	v_pk_add_f32 v[2:3], v[22:23], v[2:3]
	v_max_f32_e32 v10, 0, v10
	v_max_f32_e32 v11, 0, v11
	v_max_f32_e32 v12, 0, v12
	v_max_f32_e32 v13, 0, v13
	v_max_f32_e32 v14, 0, v14
	v_max_f32_e32 v15, 0, v15
	v_max_f32_e32 v16, 0, v16
	v_max_f32_e32 v17, 0, v17
	v_max_f32_e32 v6, 0, v6
	v_max_f32_e32 v18, 0, v7
	v_max_f32_e32 v7, 0, v8
	v_max_f32_e32 v8, 0, v9
	v_max_f32_e32 v19, 0, v2
	v_max_f32_e32 v20, 0, v3
	v_max_f32_e32 v9, 0, v4
	v_max_f32_e32 v21, 0, v5
	v_cvt_pk_f16_f32 v3, v12, v13
	v_cvt_pk_f16_f32 v2, v10, v11
	v_cvt_pk_f16_f32 v5, v16, v17
	v_cvt_pk_f16_f32 v4, v14, v15
	v_cvt_pk_f16_f32 v7, v7, v8
	v_cvt_pk_f16_f32 v6, v6, v18
	v_cvt_pk_f16_f32 v9, v9, v21
	v_cvt_pk_f16_f32 v8, v19, v20
	global_store_dwordx2 v[26:27], v[2:3], off
	global_store_dwordx2 v[0:1], v[4:5], off
	global_store_dwordx2 v[26:27], v[6:7], off offset:32
	global_store_dwordx2 v[0:1], v[8:9], off offset:32
	s_endpgm
	.p2align	8

.LBB12_11:
	s_load_dwordx2 s[2:3], s[0:1], 0x20
	s_load_dwordx2 s[4:5], s[0:1], 0x30
	v_lshlrev_b32_e32 v0, 2, v56
	v_lshl_or_b32 v0, s9, 5, v0
	v_or_b32_e32 v18, s7, v0
	v_ashrrev_i32_e32 v19, 31, v18
	v_lshlrev_b64 v[26:27], 2, v[18:19]
	s_waitcnt lgkmcnt(0)
	v_lshl_add_u64 v[28:29], s[4:5], 0, v[26:27]
	global_load_dwordx4 v[18:21], v[28:29], off
	global_load_dwordx4 v[22:25], v[28:29], off offset:64
	s_load_dword s4, s[0:1], 0x28
	s_lshl_b32 s0, s8, 5
	s_add_i32 s0, s0, s6
	v_or_b32_e32 v28, s0, v1
	v_or_b32_e32 v29, 16, v28
	v_lshl_add_u64 v[0:1], s[2:3], 0, v[26:27]
	s_waitcnt lgkmcnt(0)
	v_mad_i64_i32 v[26:27], s[0:1], v28, s4, 0
	v_mad_i64_i32 v[28:29], s[0:1], v29, s4, 0
	v_lshl_add_u64 v[26:27], v[26:27], 2, v[0:1]
	v_lshl_add_u64 v[28:29], v[28:29], 2, v[0:1]
	s_waitcnt vmcnt(0)
	v_pk_add_f32 v[12:13], v[20:21], v[12:13]
	v_pk_add_f32 v[0:1], v[18:19], v[10:11]
	v_pk_add_f32 v[10:11], v[20:21], v[16:17]
	v_pk_add_f32 v[14:15], v[18:19], v[14:15]
	v_pk_add_f32 v[16:17], v[24:25], v[8:9]
	v_pk_add_f32 v[8:9], v[22:23], v[6:7]
	v_pk_add_f32 v[18:19], v[24:25], v[4:5]
	v_pk_add_f32 v[20:21], v[22:23], v[2:3]
	v_max_f32_e32 v0, 0, v0
	v_max_f32_e32 v1, 0, v1
	v_max_f32_e32 v2, 0, v12
	v_max_f32_e32 v3, 0, v13
	v_max_f32_e32 v4, 0, v14
	v_max_f32_e32 v5, 0, v15
	v_max_f32_e32 v6, 0, v10
	v_max_f32_e32 v7, 0, v11
	v_max_f32_e32 v8, 0, v8
	v_max_f32_e32 v9, 0, v9
	v_max_f32_e32 v10, 0, v16
	v_max_f32_e32 v11, 0, v17
	v_max_f32_e32 v12, 0, v20
	v_max_f32_e32 v13, 0, v21
	v_max_f32_e32 v14, 0, v18
	v_max_f32_e32 v15, 0, v19
	global_store_dwordx4 v[26:27], v[0:3], off
	global_store_dwordx4 v[28:29], v[4:7], off
	global_store_dwordx4 v[26:27], v[8:11], off offset:64
	global_store_dwordx4 v[28:29], v[12:15], off offset:64
	s_endpgm
	.p2align	8

	.text
	.p2alignl 8, 3212836864
	.fill 256, 4, 3212836864
